# FoX loop: next-tile S accumulators rotated into place by the rank-1 (-cum) MFMA (D != C) at the loop edge instead of 16 v_mov_b64 + 5 v_mov per tile
# speedup vs baseline: 1.0175x; 1.0023x over previous
; #define GAS __attribute__((address_space(1)))
; #define LAS __attribute__((address_space(3)))
; __device__ __forceinline__ unsigned f2bf(float f) { unsigned u = __builtin_bit_cast(unsigned, f); return (u + 0x7fffu + ((u >> 16) & 1u)) >> 16; }
; #define ATT_LOAD(t) do { kreg = *(const GAS v4u*)((const char*)(Kp + (size_t)(64 * (t)) * APITCH) + lvoff); vreg = *(const GAS v4u*)((const char*)(Vp + (size_t)(64 * (t)) * APITCH) + lvoff); } while (0)
; #define ATT_STORE(slot) do { *(LAS v4u*)(kvbuf + (slot) * 16384 + kst) = kreg; *(LAS v4u*)(kvbuf + (slot) * 16384 + vst) = vreg; } while (0)
; template <int TYPE>
; __device__ __forceinline__ void causal_wg_unit(const bf16* proj, const float* cum2, const float* gn, unsigned char* obuf, int b, int h, int qb, LAS unsigned char* kvbuf, LAS float* ncum, lptr wl, LAS float* wsf, int tid, int wave) {
;     ...
;     const unsigned lvoff = (unsigned)(((tid >> 3) * APITCH + (tid & 7) * 8) * 2);
;     const int skey = tid >> 3, sch = tid & 7;
;     const int kst = sch * 1024 + ((skey ^ sch) << 4), vst = 8192 + (sch >> 2) * 4096 + ((skey ^ (sch >> 2)) << 6) + (sch & 3) * 16;
;     v4u kreg, vreg;
;     ...
;     if (TYPE == 1) { const int n = 256 * (qb + 1); if (4 * tid < n) { const f32x4 c = *(const GAS f32x4*)(cum2 + 4 * tid); v4u w;
; #pragma unroll
;         for (int e = 0; e < 4; ++e) { const float v = -c[e]; const unsigned hb = f2bf(v); const unsigned lb = f2bf(v - __builtin_bit_cast(float, hb << 16)); w[e] = hb | (lb << 16); }
;         *(LAS v4u*)(ncum + 4 * tid) = w; } }
;     const bf16x8 qone = hi ? (bf16x8){0, 0, 0, 0, 0, 0, 0, 0} : (bf16x8){(short)0x3f80, (short)0x3f80, 0, 0, 0, 0, 0, 0};
;     f32x16 o[2]; o[0] = f32x16{}; o[1] = f32x16{};
;     float mrun = -1e30f, lrun = 0.f, R = 1.f;
;     const int vbo = 8192 + ((lane >> 4) & 1) * 32 + (lane & 3) * 8 + (4 * hi + ((lane & 15) >> 2)) * 64, vsw = ((lane >> 2) & 1) ? -64 : 64;
;     ATT_LOAD(ATT_TILE(0)); ATT_STORE(0);
;     ATT_LOAD(ATT_TILE(1)); ATT_STORE(1);
;     __syncthreads();
;     f32x16 pc0 = f32x16{}, pc1 = f32x16{}, pn0 = f32x16{}, pn1 = f32x16{};
.LBB0_396:
	v_ashrrev_i32_e32 v0, 3, v124
	v_lshlrev_b32_e32 v1, 4, v143
	v_and_b32_e32 v6, 4, v167
	v_lshl_or_b32 v142, v0, 7, v1
	v_lshlrev_b32_e32 v1, 10, v143
	v_xor_b32_e32 v2, v0, v143
	v_mul_u32_u24_e32 v6, 0x110, v6
	v_lshl_add_u32 v181, v2, 4, v1
	v_lshlrev_b32_e32 v2, 12, v144
	v_xor_b32_e32 v0, v144, v0
	v_lshlrev_b32_e32 v144, 2, v124
	v_add3_u32 v133, s22, v6, v105
	v_or_b32_e32 v6, 3, v167
	v_ashrrev_i32_e32 v145, 31, v144
	v_mul_u32_u24_e32 v6, 0x110, v6
	v_lshlrev_b32_e32 v3, 6, v0
	v_lshl_add_u64 v[0:1], v[144:145], 2, s[56:57]
	v_add3_u32 v145, s22, v6, v105
	v_lshlrev_b32_e32 v6, 8, v125
	v_or_b32_e32 v4, v104, v2
	s_mov_b64 s[6:7], 0x700000
	v_add_u32_e32 v7, v141, v6
	v_lshlrev_b32_e32 v8, 6, v126
	v_add_u32_e32 v2, v2, v3
	s_add_u32 s66, s91, 0xc800
	v_lshl_add_u64 v[146:147], v[0:1], 0, s[6:7]
	v_mov_b32_e32 v97, 0
	v_add_u32_e32 v0, v4, v3
	v_lshl_add_u32 v1, v149, 10, 0
	v_lshl_add_u32 v4, v150, 10, 0
	v_lshl_add_u32 v5, v151, 10, 0
	v_add3_u32 v7, v7, v8, v127
	v_or3_b32 v6, v6, v8, v127
	v_or_b32_e32 v2, v2, v104
	s_addc_u32 s67, s92, 0
	s_mov_b32 s41, 0
	v_lshl_add_u32 v182, v124, 4, 0
	v_mov_b32_e32 v143, v97
	v_add_u32_e32 v183, 0, v105
	v_lshl_add_u32 v184, v125, 10, 0
	v_lshl_add_u32 v180, v140, 2, s86
	v_add_u32_e32 v185, 0x3e00, v7
	v_add_u32_e32 v186, 0, v148
	v_add_u32_e32 v187, 0x3c00, v7
	v_mov_b32_e32 v188, 0
	v_mov_b32_e32 v189, 0
	v_mov_b32_e32 v190, 0
	v_mov_b32_e32 v191, 0
	v_add_u32_e32 v192, 0x3200, v7
	v_add_u32_e32 v193, 0x3000, v7
	v_or_b32_e32 v194, 0x2e00, v6
	v_or_b32_e32 v195, 0x2c00, v6
	v_mov_b32_e32 v196, 0
	v_mov_b32_e32 v197, 0
	v_mov_b32_e32 v198, 0
	v_mov_b32_e32 v199, 0
	v_or_b32_e32 v200, 0x2200, v6
	v_or_b32_e32 v201, 0x2000, v6
	v_or_b32_e32 v202, 0xc100, v105
	v_add_u32_e32 v203, 0xa000, v2
	v_add_u32_e32 v204, 0x8000, v181
	s_add_i32 s93, 0, 0x21540
	s_mov_b64 s[68:69], 0x3000000
	s_movk_i32 s94, 0x7fff
	s_mov_b32 s95, 0xffff0000
	s_mov_b64 s[70:71], 0x4800000
	s_mov_b64 s[72:73], 0x6000000
	v_add_u32_e32 v205, 0, v0
	v_add_u32_e32 v206, v1, v159
	v_add_u32_e32 v207, v4, v161
	v_add_u32_e32 v208, v5, v163
	s_mov_b32 s96, 0xff800000
	v_mov_b32_e32 v209, 0x358637bd
	s_mov_b32 s97, 0xf800000
	v_mov_b32_e32 v210, 0x260
	v_mov_b32_e32 v211, 1
	v_mov_b32_e32 v212, 0xff800000
	s_and_saveexec_b64 s[98:99], s[0:1]
	v_mov_b32_e32 v239, 0
	v_mov_b32_e32 v240, 1
	global_atomic_add v238, v239, v240, s[66:67] sc0
	s_mov_b64 exec, s[98:99]
	s_branch .LBB0_399

.LBB0_413:
	s_add_i32 s46, s47, 1
	s_cmp_ge_u32 s46, s61
	s_cselect_b64 s[6:7], -1, 0
	s_cmp_ge_u32 s47, s63
	s_cselect_b64 s[8:9], -1, 0
	s_or_b64 s[6:7], s[8:9], s[6:7]
	s_and_b64 vcc, exec, s[6:7]
	s_cbranch_vccnz .LBB0_423
	v_mov_b32_e32 v196, 0
	v_add_u32_e32 v48, 0, v213
	v_mov_b32_e32 v188, 0
	s_and_saveexec_b64 s[6:7], s[4:5]
	ds_read_b32 v188, v48
	s_or_b64 exec, exec, s[6:7]
	s_and_saveexec_b64 s[6:7], s[4:5]
	ds_read_b32 v196, v48 offset:128
	s_or_b64 exec, exec, s[6:7]
	s_mul_hi_u32 s6, s62, 0xaaaaaaab
	s_lshr_b32 s6, s6, 1
	s_mul_i32 s6, s6, 0xc000
	v_subrev_u32_e32 v68, s6, v157
	v_add_u32_e32 v96, s60, v184
	v_add_u32_e32 v98, v96, v68
	ds_read_b128 v[218:221], v98 offset:16384
	ds_read_b128 v[222:225], v98 offset:16896
	v_subrev_u32_e32 v98, s6, v159
	v_add_u32_e32 v98, v96, v98
	s_waitcnt lgkmcnt(1)
	v_mfma_f32_32x32x16_bf16 v[48:63], v[218:221], v[108:111], 0
	s_waitcnt lgkmcnt(0)
	v_mfma_f32_32x32x16_bf16 v[64:79], v[222:225], v[108:111], 0
	ds_read_b128 v[218:221], v98 offset:18432
	ds_read_b128 v[222:225], v98 offset:18944
	v_subrev_u32_e32 v98, s6, v161
	v_add_u32_e32 v98, v96, v98
	s_waitcnt lgkmcnt(1)
	v_mfma_f32_32x32x16_bf16 v[48:63], v[218:221], v[100:103], v[48:63]
	s_waitcnt lgkmcnt(0)
	v_mfma_f32_32x32x16_bf16 v[64:79], v[222:225], v[100:103], v[64:79]
	ds_read_b128 v[218:221], v98 offset:20480
	ds_read_b128 v[222:225], v98 offset:20992
	v_subrev_u32_e32 v98, s6, v163
	v_add_u32_e32 v96, v96, v98
	s_waitcnt lgkmcnt(1)
	v_mfma_f32_32x32x16_bf16 v[48:63], v[218:221], v[104:107], v[48:63]
	s_waitcnt lgkmcnt(0)
	v_mfma_f32_32x32x16_bf16 v[64:79], v[222:225], v[104:107], v[64:79]
	ds_read_b128 v[218:221], v96 offset:22528
	ds_read_b128 v[222:225], v96 offset:23040
	s_waitcnt lgkmcnt(1)
	v_mfma_f32_32x32x16_bf16 v[48:63], v[218:221], v[112:115], v[48:63]
	s_waitcnt lgkmcnt(0)
	v_mfma_f32_32x32x16_bf16 v[64:79], v[222:225], v[112:115], v[64:79]
	s_cmp_gt_u32 s47, s63
	s_cbranch_scc0 .LBB0_424

; #define LAS __attribute__((address_space(3)))
; template <int TYPE>
; __device__ __forceinline__ void causal_wg_unit(const bf16* proj, const float* cum2, const float* gn, unsigned char* obuf, int b, int h, int qb, LAS unsigned char* kvbuf, LAS float* ncum, lptr wl, LAS float* wsf, int tid, int wave) {
;     ...
;         if (TYPE == 0) { const v4u f0 = *(const LAS v4u*)(aflag + (s & 1) * 8), f1 = *(const LAS v4u*)(aflag + (s & 1) * 8 + 4);
;             if (((f0.x | f0.y) | (f0.z | f0.w) | (f1.x | f1.y) | (f1.z | f1.w)) == 0u) break; }
;         pc0 = pn0; pc1 = pn1;
;     }
.LBB0_421:
	s_add_i32 s40, s40, 64
	s_addk_i32 s60, 0x4000
	s_add_i32 s62, s62, 1
	s_add_i32 s33, s33, 1
	s_cmp_eq_u32 s61, s46
	v_add_u32_e32 v213, 0x100, v213
	s_waitcnt lgkmcnt(0)
	s_barrier
	s_cbranch_scc1 .LBB0_433
	v_mfma_f32_32x32x16_bf16 v[80:95], v[188:191], v[124:127], v[48:63]
	v_mfma_f32_32x32x16_bf16 v[32:47], v[196:199], v[124:127], v[64:79]
	s_mov_b32 s47, s46
	s_branch .LBB0_411

; #define GAS __attribute__((address_space(1)))
; #define LAS __attribute__((address_space(3)))
; __device__ __forceinline__ unsigned f2bf(float f) { unsigned u = __builtin_bit_cast(unsigned, f); return (u + 0x7fffu + ((u >> 16) & 1u)) >> 16; }
; #define ATT_LOAD(t) do { kreg = *(const GAS v4u*)((const char*)(Kp + (size_t)(64 * (t)) * APITCH) + lvoff); vreg = *(const GAS v4u*)((const char*)(Vp + (size_t)(64 * (t)) * APITCH) + lvoff); } while (0)
; #define ATT_STORE(slot) do { *(LAS v4u*)(kvbuf + (slot) * 16384 + kst) = kreg; *(LAS v4u*)(kvbuf + (slot) * 16384 + vst) = vreg; } while (0)
; template <int TYPE>
; __device__ __forceinline__ void causal_wg_unit(const bf16* proj, const float* cum2, const float* gn, unsigned char* obuf, int b, int h, int qb, LAS unsigned char* kvbuf, LAS float* ncum, lptr wl, LAS float* wsf, int tid, int wave) {
;     ...
;     const unsigned lvoff = (unsigned)(((tid >> 3) * APITCH + (tid & 7) * 8) * 2);
;     const int skey = tid >> 3, sch = tid & 7;
;     const int kst = sch * 1024 + ((skey ^ sch) << 4), vst = 8192 + (sch >> 2) * 4096 + ((skey ^ (sch >> 2)) << 6) + (sch & 3) * 16;
;     v4u kreg, vreg;
;     ...
;     if (TYPE == 1) { const int n = 256 * (qb + 1); if (4 * tid < n) { const f32x4 c = *(const GAS f32x4*)(cum2 + 4 * tid); v4u w;
; #pragma unroll
;         for (int e = 0; e < 4; ++e) { const float v = -c[e]; const unsigned hb = f2bf(v); const unsigned lb = f2bf(v - __builtin_bit_cast(float, hb << 16)); w[e] = hb | (lb << 16); }
;         *(LAS v4u*)(ncum + 4 * tid) = w; } }
;     const bf16x8 qone = hi ? (bf16x8){0, 0, 0, 0, 0, 0, 0, 0} : (bf16x8){(short)0x3f80, (short)0x3f80, 0, 0, 0, 0, 0, 0};
;     f32x16 o[2]; o[0] = f32x16{}; o[1] = f32x16{};
;     float mrun = -1e30f, lrun = 0.f, R = 1.f;
;     const int vbo = 8192 + ((lane >> 4) & 1) * 32 + (lane & 3) * 8 + (4 * hi + ((lane & 15) >> 2)) * 64, vsw = ((lane >> 2) & 1) ? -64 : 64;
;     ATT_LOAD(ATT_TILE(0)); ATT_STORE(0);
;     ATT_LOAD(ATT_TILE(1)); ATT_STORE(1);
;     __syncthreads();
;     f32x16 pc0 = f32x16{}, pc1 = f32x16{}, pn0 = f32x16{}, pn1 = f32x16{};
.LBB0_1306:
	v_ashrrev_i32_e32 v0, 3, v124
	v_lshlrev_b32_e32 v1, 4, v143
	v_and_b32_e32 v6, 4, v167
	v_lshl_or_b32 v142, v0, 7, v1
	v_lshlrev_b32_e32 v1, 10, v143
	v_xor_b32_e32 v2, v0, v143
	v_mul_u32_u24_e32 v6, 0x110, v6
	v_lshl_add_u32 v181, v2, 4, v1
	v_lshlrev_b32_e32 v2, 12, v144
	v_xor_b32_e32 v0, v144, v0
	v_lshlrev_b32_e32 v144, 2, v124
	v_add3_u32 v133, s22, v6, v105
	v_or_b32_e32 v6, 3, v167
	v_ashrrev_i32_e32 v145, 31, v144
	v_mul_u32_u24_e32 v6, 0x110, v6
	v_lshlrev_b32_e32 v3, 6, v0
	v_lshl_add_u64 v[0:1], v[144:145], 2, s[56:57]
	v_add3_u32 v145, s22, v6, v105
	v_lshlrev_b32_e32 v6, 8, v125
	v_or_b32_e32 v4, v104, v2
	s_mov_b64 s[6:7], 0x700000
	v_add_u32_e32 v7, v141, v6
	v_lshlrev_b32_e32 v8, 6, v126
	v_add_u32_e32 v2, v2, v3
	s_add_u32 s66, s90, 0xe800
	v_lshl_add_u64 v[146:147], v[0:1], 0, s[6:7]
	v_mov_b32_e32 v97, 0
	v_add_u32_e32 v0, v4, v3
	v_lshl_add_u32 v1, v149, 10, 0
	v_lshl_add_u32 v4, v150, 10, 0
	v_lshl_add_u32 v5, v151, 10, 0
	v_add3_u32 v7, v7, v8, v127
	v_or3_b32 v6, v6, v8, v127
	v_or_b32_e32 v2, v2, v104
	s_addc_u32 s67, s91, 0
	s_mov_b32 s41, 0
	v_lshl_add_u32 v182, v124, 4, 0
	v_mov_b32_e32 v143, v97
	v_add_u32_e32 v183, 0, v105
	v_lshl_add_u32 v184, v125, 10, 0
	v_lshl_add_u32 v180, v140, 2, s82
	v_add_u32_e32 v185, 0x3e00, v7
	v_add_u32_e32 v186, 0, v148
	v_add_u32_e32 v187, 0x3c00, v7
	v_mov_b32_e32 v188, 0
	v_mov_b32_e32 v189, 0
	v_mov_b32_e32 v190, 0
	v_mov_b32_e32 v191, 0
	v_add_u32_e32 v192, 0x3200, v7
	v_add_u32_e32 v193, 0x3000, v7
	v_or_b32_e32 v194, 0x2e00, v6
	v_or_b32_e32 v195, 0x2c00, v6
	v_mov_b32_e32 v196, 0
	v_mov_b32_e32 v197, 0
	v_mov_b32_e32 v198, 0
	v_mov_b32_e32 v199, 0
	v_or_b32_e32 v200, 0x2200, v6
	v_or_b32_e32 v201, 0x2000, v6
	v_or_b32_e32 v202, 0xc100, v105
	v_add_u32_e32 v203, 0xa000, v2
	v_add_u32_e32 v204, 0x8000, v181
	s_add_i32 s92, 0, 0x21540
	s_mov_b64 s[68:69], 0x3000000
	s_movk_i32 s93, 0x7fff
	s_mov_b32 s94, 0xffff0000
	s_mov_b64 s[70:71], 0x4800000
	s_mov_b64 s[72:73], 0x6000000
	v_add_u32_e32 v205, 0, v0
	v_add_u32_e32 v206, v1, v159
	v_add_u32_e32 v207, v4, v161
	v_add_u32_e32 v208, v5, v163
	s_mov_b32 s95, 0xff800000
	v_mov_b32_e32 v209, 0x358637bd
	s_mov_b32 s96, 0xf800000
	v_mov_b32_e32 v210, 0x260
	v_mov_b32_e32 v211, 1
	v_mov_b32_e32 v212, 0xff800000
	s_and_saveexec_b64 s[98:99], s[0:1]
	v_mov_b32_e32 v239, 0
	v_mov_b32_e32 v240, 1
	global_atomic_add v238, v239, v240, s[66:67] sc0
	s_mov_b64 exec, s[98:99]
	s_branch .LBB0_1309
